# MLA steady loops: both wave groups issue their LDS-DMA pieces behind the first QK MFMAs
# baseline (speedup 1.0000x reference)
; #define SFENCE() __builtin_amdgcn_sched_barrier(0)
; template <bool FOX>
; __device__ __forceinline__ void attn_unit(const Args& A, int b, int h, int qb, LAS char* shm, LAS float* dg) {
;     ...
;           const lds_cptr vp = vp0 + ((t - 1) % NS) * VSLOT; float sa = 0.f, sb = 0.f;
; #pragma unroll
;           for (int g = 0; g < 2 * NQ; ++g) {
;               if (!FOX && g == 0) c0 = __builtin_amdgcn_mfma_f32_32x32x16_bf16(kf[0], qr[0], negm, 0, 0, 0);
;               else if (!FOX && g == 1) c1 = __builtin_amdgcn_mfma_f32_32x32x16_bf16(kf[1], qr[0], negm, 0, 0, 0);
;               else if (g & 1) c1 = __builtin_amdgcn_mfma_f32_32x32x16_bf16(kf[g], qr[g >> 1], c1, 0, 0, 0); else c0 = __builtin_amdgcn_mfma_f32_32x32x16_bf16(kf[g], qr[g >> 1], c0, 0, 0, 0);
;               if (g < 8) { const int i = (g >> 1) + 4 * (g & 1); vlo[i] = vtr(vp + (i >> 2) * 4096 + (i & 3) * 1024); vhi[i] = vtr(vp + (i >> 2) * 4096 + (i & 3) * 1024 + 512);
;                   if (g < 4) { sa += pp0[4 * g]; sb += pp0[4 * g + 1]; sa += pp0[4 * g + 2]; sb += pp0[4 * g + 3]; } else { sa += pp1[4 * g - 16]; sb += pp1[4 * g - 15]; sa += pp1[4 * g - 14]; sb += pp1[4 * g - 13]; }
;                   asm volatile("" : "+v"(sa), "+v"(sb)); }
;               { constexpr int G0 = FOX ? 0 : 4; if (g >= G0) { const int q = 2 * (g - G0);
; #pragma unroll
;                   for (int k = 0; k < 2; ++k) { const int w = q + k; const unsigned pkd = w < 8 ? cvt_pk_bf16(pp0[2 * w], pp0[2 * w + 1]) : cvt_pk_bf16(pp1[2 * w - 16], pp1[2 * w - 15]); pw[w >> 2][w & 3] = pkd; } } }
;               SFENCE();
;           }
;           lrun += sa + sb; }
;         MASKONLY(t);
;         float rm; ROWMAX(rm);
;         bool resc = false;
;         if (__any(rm > THR)) { const float dl = fmaxf(rm, 0.f); mhat += dl;
; #pragma unroll
;             for (int r = 0; r < 16; ++r) { c0[r] -= dl; c1[r] -= dl; }
;             if constexpr (!FOX) {
; #pragma unroll
;                 for (int r = 0; r < 16; ++r) negm[r] = -mhat;
;                 asm volatile("" : "+v"(negm)); }
;             const float f = __builtin_amdgcn_exp2f(-dl); lrun *= f; if (hi == 0) wsf[r32] = f; resc = true; }
;         SFENCE();
;         { const lds_cptr kp = kp0 + ((t + 1) % NS) * KSLOT;
; #pragma unroll
;           for (int g = 0; g < 8; ++g) { const int i = (g >> 1) + 4 * (g & 1);
.Lmla_ss2_top:
	s_mov_b32 m0, s52
	s_waitcnt lgkmcnt(0)
	s_add_i32 s27, s42, 0x8000
	v_mfma_f32_32x32x16_bf16 v[114:129], v[206:209], v[138:141], v[82:97]
	global_load_lds_dwordx4 v[234:235], off
	s_mov_b32 m0, s53
	s_and_b32 s27, s27, 0x6000
	s_add_u32 s42, s42, 0x2000
	s_addc_u32 s43, s43, 0
	v_add_u32_e32 v3, s27, v247
	ds_read_b64_tr_b16 v[206:207], v3 offset:49152
	ds_read_b64_tr_b16 v[208:209], v3 offset:49664
	v_add_f32_e32 v4, 0, v67
	v_add_f32_e32 v5, 0, v66
	v_add_f32_e32 v4, v69, v4
	v_add_f32_e32 v5, v68, v5
	v_mfma_f32_32x32x16_bf16 v[98:113], v[194:197], v[138:141], v[82:97]
	global_load_lds_dwordx4 v[250:251], off
	ds_read_b64_tr_b16 v[194:195], v3 offset:53248
	ds_read_b64_tr_b16 v[196:197], v3 offset:53760
	v_add_f32_e32 v4, v71, v4
	v_add_f32_e32 v5, v70, v5
	v_add_f32_e32 v4, v73, v4
	v_add_f32_e32 v5, v72, v5
	v_mfma_f32_32x32x16_bf16 v[114:129], v[202:205], v[142:145], v[114:129]
	ds_read_b64_tr_b16 v[202:203], v3 offset:50176
	ds_read_b64_tr_b16 v[204:205], v3 offset:50688
	v_add_f32_e32 v4, v75, v4
	v_add_f32_e32 v5, v74, v5
	v_add_f32_e32 v4, v77, v4
	v_add_f32_e32 v5, v76, v5
	v_mfma_f32_32x32x16_bf16 v[98:113], v[186:189], v[142:145], v[98:113]
	ds_read_b64_tr_b16 v[214:215], v3 offset:54272
	ds_read_b64_tr_b16 v[216:217], v3 offset:54784
	v_add_f32_e32 v4, v79, v4
	v_add_f32_e32 v5, v78, v5
	v_add_f32_e32 v4, v81, v4
	v_add_f32_e32 v5, v80, v5
	v_mfma_f32_32x32x16_bf16 v[114:129], v[198:201], v[146:149], v[114:129]
	ds_read_b64_tr_b16 v[210:211], v3 offset:51200
	ds_read_b64_tr_b16 v[212:213], v3 offset:51712
	v_add_f32_e32 v4, v51, v4
	v_add_f32_e32 v5, v50, v5
	v_add_f32_e32 v4, v53, v4
	v_add_f32_e32 v5, v52, v5
	v_mfma_f32_32x32x16_bf16 v[98:113], v[182:185], v[146:149], v[98:113]
	ds_read_b64_tr_b16 v[12:13], v3 offset:55296
	ds_read_b64_tr_b16 v[14:15], v3 offset:55808
	v_add_f32_e32 v4, v55, v4
	v_add_f32_e32 v5, v54, v5
	v_add_f32_e32 v4, v57, v4
	v_add_f32_e32 v5, v56, v5
	v_mfma_f32_32x32x16_bf16 v[114:129], v[190:193], v[150:153], v[114:129]
	ds_read_b64_tr_b16 v[8:9], v3 offset:52224
	ds_read_b64_tr_b16 v[10:11], v3 offset:52736
	v_add_f32_e32 v4, v59, v4
	v_add_f32_e32 v16, v61, v4
	v_add_f32_e32 v4, v58, v5
	v_add_f32_e32 v17, v60, v4
	v_mfma_f32_32x32x16_bf16 v[98:113], v[170:173], v[150:153], v[98:113]
	v_lshl_add_u64 v[234:235], v[234:235], 0, s[62:63]
	s_and_b32 s64, s26, 3
	ds_read_b64_tr_b16 v[4:5], v3 offset:56320
	ds_read_b64_tr_b16 v[6:7], v3 offset:56832
	v_add_f32_e32 v3, v63, v16
	v_add_f32_e32 v16, v62, v17
	v_add_f32_e32 v3, v65, v3
	v_add_f32_e32 v16, v64, v16
	v_mfma_f32_32x32x16_bf16 v[114:129], v[178:181], v[154:157], v[114:129]
	s_mulk_i32 s64, 0x3000
	v_lshl_add_u64 v[250:251], v[232:233], 0, s[42:43]
	v_cvt_pk_bf16_f32 v178, v50, v51
	v_cvt_pk_bf16_f32 v179, v52, v53
	v_cvt_pk_bf16_f32 v186, v66, v67
	v_cvt_pk_bf16_f32 v187, v68, v69
	v_mfma_f32_32x32x16_bf16 v[98:113], v[166:169], v[154:157], v[98:113]
	s_add_i32 s52, s64, s91
	s_add_i32 s64, s42, 0x6000
	v_cvt_pk_bf16_f32 v180, v54, v55
	v_cvt_pk_bf16_f32 v181, v56, v57
	v_cvt_pk_bf16_f32 v188, v70, v71
	v_cvt_pk_bf16_f32 v189, v72, v73
	v_mfma_f32_32x32x16_bf16 v[114:129], v[174:177], v[158:161], v[114:129]
	s_and_b32 s64, s64, 0x6000
	s_add_i32 s53, s64, s93
	v_cvt_pk_bf16_f32 v218, v58, v59
	v_cvt_pk_bf16_f32 v219, v60, v61
	v_cvt_pk_bf16_f32 v182, v74, v75
	v_cvt_pk_bf16_f32 v183, v76, v77
	v_mfma_f32_32x32x16_bf16 v[98:113], v[162:165], v[158:161], v[98:113]
	v_cvt_pk_bf16_f32 v220, v62, v63
	v_cvt_pk_bf16_f32 v221, v64, v65
	v_cvt_pk_bf16_f32 v184, v78, v79
	v_cvt_pk_bf16_f32 v185, v80, v81
	v_add_f32_e32 v3, v3, v16
	v_add_f32_e32 v246, v246, v3
	s_waitcnt vmcnt(3)
	s_waitcnt lgkmcnt(0)
	s_barrier
	v_mfma_f32_32x32x16_bf16 v[18:33], v[186:189], v[206:209], v[18:33]
	s_add_i32 s27, s26, 1
	s_and_b32 s64, s27, 3
	s_mulk_i32 s64, 0x3000
	v_exp_f32_e32 v66, v114
	v_exp_f32_e32 v67, v115
	v_exp_f32_e32 v68, v116
	v_exp_f32_e32 v69, v117
	v_add_u32_e32 v3, s64, v248
	v_mfma_f32_32x32x16_bf16 v[34:49], v[186:189], v[194:197], v[34:49]
	v_exp_f32_e32 v70, v118
	v_exp_f32_e32 v71, v119
	v_exp_f32_e32 v72, v120
	v_exp_f32_e32 v73, v121
	ds_read_b128 v[206:209], v3
	ds_read_b128 v[194:197], v3 offset:512
	v_mfma_f32_32x32x16_bf16 v[18:33], v[182:185], v[202:205], v[18:33]
	v_exp_f32_e32 v74, v122
	v_exp_f32_e32 v75, v123
	v_exp_f32_e32 v76, v124
	v_exp_f32_e32 v77, v125
	ds_read_b128 v[202:205], v3 offset:2048
	ds_read_b128 v[186:189], v3 offset:2560
	v_mfma_f32_32x32x16_bf16 v[34:49], v[182:185], v[214:217], v[34:49]
	v_exp_f32_e32 v78, v126
	v_exp_f32_e32 v79, v127
	v_exp_f32_e32 v80, v128
	v_exp_f32_e32 v81, v129
	ds_read_b128 v[198:201], v3 offset:4096
	ds_read_b128 v[182:185], v3 offset:4608
	v_mfma_f32_32x32x16_bf16 v[18:33], v[178:181], v[210:213], v[18:33]
	v_exp_f32_e32 v50, v98
	v_exp_f32_e32 v51, v99
	v_exp_f32_e32 v52, v100
	v_exp_f32_e32 v53, v101
	ds_read_b128 v[190:193], v3 offset:6144
	ds_read_b128 v[170:173], v3 offset:6656
	v_mfma_f32_32x32x16_bf16 v[34:49], v[178:181], v[12:15], v[34:49]
	v_exp_f32_e32 v54, v102
	v_exp_f32_e32 v55, v103
	v_exp_f32_e32 v56, v104
	v_exp_f32_e32 v57, v105
	ds_read_b128 v[178:181], v3 offset:8192
	ds_read_b128 v[166:169], v3 offset:8704
	v_mfma_f32_32x32x16_bf16 v[18:33], v[218:221], v[8:11], v[18:33]
	v_exp_f32_e32 v58, v106
	v_exp_f32_e32 v59, v107
	v_exp_f32_e32 v60, v108
	v_exp_f32_e32 v61, v109
	ds_read_b128 v[174:177], v3 offset:10240
	ds_read_b128 v[162:165], v3 offset:10752
	v_mfma_f32_32x32x16_bf16 v[34:49], v[218:221], v[4:7], v[34:49]
	v_exp_f32_e32 v62, v110
	v_exp_f32_e32 v63, v111
	v_exp_f32_e32 v64, v112
	v_exp_f32_e32 v65, v113
	s_mov_b32 s26, s27
	s_cmp_eq_u32 s27, s96
	s_cbranch_scc1 .Lmla_ss2_xdone
	s_add_i32 s64, s27, 3
	s_cmp_lt_u32 s64, s94
	s_cbranch_scc1 .Lmla_ss2_top
	s_branch .Lmla_ss_back
